# skip tests use one v_cmp against per-chunk threshold M-26 (strict >), removing 16 v_sub per head; results identical (2^-26 probabilities round to 0 in f16 either way)
# baseline (speedup 1.0000x reference)
.LBB1_20:
	v_max3_f32 v3, v1, v243, v241
	v_max3_f32 v3, v3, v242, v239
	v_max3_f32 v3, v3, v240, v237
	v_max_f32_e32 v3, v3, v238
	v_mov_b32_e32 v4, v3
	s_nop 1
	v_permlane32_swap_b32_e32 v3, v4
	v_max3_f32 v236, v3, v4, s43
	v_add_f32_e32 v244, s56, v236
	s_setprio 1
	v_cmp_lt_f32_e32 vcc, v244, v1
	s_cbranch_vccz .LBB1_82
	ds_read_b128 v[10:13], v206 offset:49152
	v_sub_f32_e32 v1, v66, v236
	v_sub_f32_e32 v3, v68, v236
	v_sub_f32_e32 v5, v70, v236
	v_sub_f32_e32 v7, v72, v236
	v_exp_f32_e32 v14, v1
	v_sub_f32_e32 v1, v67, v236
	v_exp_f32_e32 v4, v3
	v_sub_f32_e32 v3, v69, v236
	v_exp_f32_e32 v6, v5
	v_sub_f32_e32 v5, v71, v236
	v_exp_f32_e32 v8, v7
	v_sub_f32_e32 v7, v73, v236
	v_exp_f32_e32 v7, v7
	v_exp_f32_e32 v5, v5
	v_exp_f32_e32 v3, v3
	v_exp_f32_e32 v1, v1
	v_cvt_pk_f16_f32 v9, v8, v7
	v_cvt_pk_f16_f32 v8, v6, v5
	v_cvt_pk_f16_f32 v7, v4, v3
	v_cvt_pk_f16_f32 v6, v14, v1
	s_waitcnt lgkmcnt(0)
	s_nop 0
	v_mfma_f32_32x32x16_f16 v[98:113], v[10:13], v[6:9], 0
	v_mfma_f32_32x32x16_f16 v[82:97], v[194:197], v[6:9], 0
	v_cmp_lt_f32_e32 vcc, v244, v243
	s_cbranch_vccz .LBB1_23

.LBB1_23:
	v_cmp_lt_f32_e32 vcc, v244, v242
	s_cbranch_vccz .LBB1_83
	ds_read_b128 v[10:13], v206 offset:51200
	v_sub_f32_e32 v1, v50, v236
	v_sub_f32_e32 v3, v52, v236
	v_sub_f32_e32 v5, v54, v236
	v_sub_f32_e32 v7, v56, v236
	v_exp_f32_e32 v14, v1
	v_sub_f32_e32 v1, v51, v236
	v_exp_f32_e32 v4, v3
	v_sub_f32_e32 v3, v53, v236
	v_exp_f32_e32 v6, v5
	v_sub_f32_e32 v5, v55, v236
	v_exp_f32_e32 v8, v7
	v_sub_f32_e32 v7, v57, v236
	v_exp_f32_e32 v7, v7
	v_exp_f32_e32 v5, v5
	v_exp_f32_e32 v3, v3
	v_exp_f32_e32 v1, v1
	v_cvt_pk_f16_f32 v9, v8, v7
	v_cvt_pk_f16_f32 v8, v6, v5
	v_cvt_pk_f16_f32 v7, v4, v3
	v_cvt_pk_f16_f32 v6, v14, v1
	s_waitcnt lgkmcnt(0)
	s_nop 0
	v_mfma_f32_32x32x16_f16 v[98:113], v[10:13], v[6:9], v[98:113]
	v_mfma_f32_32x32x16_f16 v[82:97], v[194:197], v[6:9], v[82:97]
	v_cmp_lt_f32_e32 vcc, v244, v241
	s_cbranch_vccz .LBB1_26

.LBB1_26:
	v_cmp_lt_f32_e32 vcc, v244, v240
	s_cbranch_vccz .LBB1_84
	ds_read_b128 v[10:13], v206 offset:53248
	v_sub_f32_e32 v1, v34, v236
	v_sub_f32_e32 v3, v36, v236
	v_sub_f32_e32 v5, v38, v236
	v_sub_f32_e32 v7, v40, v236
	v_exp_f32_e32 v14, v1
	v_sub_f32_e32 v1, v35, v236
	v_exp_f32_e32 v4, v3
	v_sub_f32_e32 v3, v37, v236
	v_exp_f32_e32 v6, v5
	v_sub_f32_e32 v5, v39, v236
	v_exp_f32_e32 v8, v7
	v_sub_f32_e32 v7, v41, v236
	v_exp_f32_e32 v7, v7
	v_exp_f32_e32 v5, v5
	v_exp_f32_e32 v3, v3
	v_exp_f32_e32 v1, v1
	v_cvt_pk_f16_f32 v9, v8, v7
	v_cvt_pk_f16_f32 v8, v6, v5
	v_cvt_pk_f16_f32 v7, v4, v3
	v_cvt_pk_f16_f32 v6, v14, v1
	s_waitcnt lgkmcnt(0)
	s_nop 0
	v_mfma_f32_32x32x16_f16 v[98:113], v[10:13], v[6:9], v[98:113]
	v_mfma_f32_32x32x16_f16 v[82:97], v[194:197], v[6:9], v[82:97]
	v_cmp_lt_f32_e32 vcc, v244, v239
	s_cbranch_vccz .LBB1_29

.LBB1_29:
	v_cmp_lt_f32_e32 vcc, v244, v238
	s_cbranch_vccz .LBB1_85
	ds_read_b128 v[10:13], v206 offset:55296
	v_sub_f32_e32 v1, v18, v236
	v_sub_f32_e32 v3, v20, v236
	v_sub_f32_e32 v5, v22, v236
	v_sub_f32_e32 v7, v24, v236
	v_exp_f32_e32 v14, v1
	v_sub_f32_e32 v1, v19, v236
	v_exp_f32_e32 v4, v3
	v_sub_f32_e32 v3, v21, v236
	v_exp_f32_e32 v6, v5
	v_sub_f32_e32 v5, v23, v236
	v_exp_f32_e32 v8, v7
	v_sub_f32_e32 v7, v25, v236
	v_exp_f32_e32 v7, v7
	v_exp_f32_e32 v5, v5
	v_exp_f32_e32 v3, v3
	v_exp_f32_e32 v1, v1
	v_cvt_pk_f16_f32 v9, v8, v7
	v_cvt_pk_f16_f32 v8, v6, v5
	v_cvt_pk_f16_f32 v7, v4, v3
	v_cvt_pk_f16_f32 v6, v14, v1
	s_waitcnt lgkmcnt(0)
	s_nop 0
	v_mfma_f32_32x32x16_f16 v[98:113], v[10:13], v[6:9], v[98:113]
	v_mfma_f32_32x32x16_f16 v[82:97], v[194:197], v[6:9], v[82:97]
	v_cmp_lt_f32_e32 vcc, v244, v237
	s_cbranch_vccz .LBB1_32

.LBB1_47:
	v_max3_f32 v3, v1, v16, v14
	v_max3_f32 v3, v3, v15, v12
	v_max3_f32 v3, v3, v13, v9
	v_max_f32_e32 v3, v3, v11
	v_mov_b32_e32 v4, v3
	s_nop 1
	v_permlane32_swap_b32_e32 v3, v4
	v_max3_f32 v10, v236, v3, v4
	v_add_f32_e32 v244, s56, v10
	v_sub_f32_e32 v3, v236, v10
	v_exp_f32_e32 v4, v3
	s_nop 0
	v_mul_f32_e32 v82, v82, v4
	v_pk_mul_f32 v[112:113], v[4:5], v[112:113] op_sel_hi:[0,1]
	v_pk_mul_f32 v[110:111], v[4:5], v[110:111] op_sel_hi:[0,1]
	v_pk_mul_f32 v[108:109], v[4:5], v[108:109] op_sel_hi:[0,1]
	v_pk_mul_f32 v[106:107], v[4:5], v[106:107] op_sel_hi:[0,1]
	v_pk_mul_f32 v[104:105], v[4:5], v[104:105] op_sel_hi:[0,1]
	v_pk_mul_f32 v[102:103], v[4:5], v[102:103] op_sel_hi:[0,1]
	v_pk_mul_f32 v[100:101], v[4:5], v[100:101] op_sel_hi:[0,1]
	v_pk_mul_f32 v[98:99], v[4:5], v[98:99] op_sel_hi:[0,1]
	s_setprio 1
	v_cmp_lt_f32_e32 vcc, v244, v1
	s_cbranch_vccz .LBB1_86
	ds_read_b128 v[114:117], v206 offset:57344
	v_sub_f32_e32 v1, v66, v10
	v_sub_f32_e32 v3, v68, v10
	v_sub_f32_e32 v5, v70, v10
	v_sub_f32_e32 v7, v72, v10
	v_exp_f32_e32 v17, v1
	v_sub_f32_e32 v1, v67, v10
	v_exp_f32_e32 v4, v3
	v_sub_f32_e32 v3, v69, v10
	v_exp_f32_e32 v6, v5
	v_sub_f32_e32 v5, v71, v10
	v_exp_f32_e32 v8, v7
	v_sub_f32_e32 v7, v73, v10
	v_exp_f32_e32 v7, v7
	v_exp_f32_e32 v5, v5
	v_exp_f32_e32 v3, v3
	v_exp_f32_e32 v1, v1
	v_cvt_pk_f16_f32 v239, v8, v7
	v_cvt_pk_f16_f32 v238, v6, v5
	v_cvt_pk_f16_f32 v237, v4, v3
	v_cvt_pk_f16_f32 v236, v17, v1
	s_waitcnt lgkmcnt(0)
	s_nop 0
	v_mfma_f32_32x32x16_f16 v[98:113], v[114:117], v[236:239], v[98:113]
	v_mfma_f32_32x32x16_f16 v[82:97], v[194:197], v[236:239], v[82:97]
	v_cmp_lt_f32_e32 vcc, v244, v16
	s_cbranch_vccz .LBB1_50

.LBB1_50:
	v_cmp_lt_f32_e32 vcc, v244, v15
	s_cbranch_vccz .LBB1_87
	ds_read_b128 v[114:117], v206 offset:59392
	v_sub_f32_e32 v1, v50, v10
	v_sub_f32_e32 v3, v52, v10
	v_sub_f32_e32 v5, v54, v10
	v_sub_f32_e32 v7, v56, v10
	v_exp_f32_e32 v15, v1
	v_sub_f32_e32 v1, v51, v10
	v_exp_f32_e32 v4, v3
	v_sub_f32_e32 v3, v53, v10
	v_exp_f32_e32 v6, v5
	v_sub_f32_e32 v5, v55, v10
	v_exp_f32_e32 v8, v7
	v_sub_f32_e32 v7, v57, v10
	v_exp_f32_e32 v7, v7
	v_exp_f32_e32 v5, v5
	v_exp_f32_e32 v3, v3
	v_exp_f32_e32 v1, v1
	v_cvt_pk_f16_f32 v239, v8, v7
	v_cvt_pk_f16_f32 v238, v6, v5
	v_cvt_pk_f16_f32 v237, v4, v3
	v_cvt_pk_f16_f32 v236, v15, v1
	s_waitcnt lgkmcnt(0)
	s_nop 0
	v_mfma_f32_32x32x16_f16 v[98:113], v[114:117], v[236:239], v[98:113]
	v_mfma_f32_32x32x16_f16 v[82:97], v[194:197], v[236:239], v[82:97]
	v_cmp_lt_f32_e32 vcc, v244, v14
	s_cbranch_vccz .LBB1_53

.LBB1_53:
	v_cmp_lt_f32_e32 vcc, v244, v13
	s_cbranch_vccz .LBB1_88
	ds_read_b128 v[14:17], v206 offset:61440
	v_sub_f32_e32 v1, v34, v10
	v_sub_f32_e32 v3, v36, v10
	v_sub_f32_e32 v5, v38, v10
	v_sub_f32_e32 v7, v40, v10
	v_exp_f32_e32 v13, v1
	v_sub_f32_e32 v1, v35, v10
	v_exp_f32_e32 v4, v3
	v_sub_f32_e32 v3, v37, v10
	v_exp_f32_e32 v6, v5
	v_sub_f32_e32 v5, v39, v10
	v_exp_f32_e32 v8, v7
	v_sub_f32_e32 v7, v41, v10
	v_exp_f32_e32 v7, v7
	v_exp_f32_e32 v5, v5
	v_exp_f32_e32 v3, v3
	v_exp_f32_e32 v1, v1
	v_cvt_pk_f16_f32 v239, v8, v7
	v_cvt_pk_f16_f32 v238, v6, v5
	v_cvt_pk_f16_f32 v237, v4, v3
	v_cvt_pk_f16_f32 v236, v13, v1
	s_waitcnt lgkmcnt(0)
	s_nop 0
	v_mfma_f32_32x32x16_f16 v[98:113], v[14:17], v[236:239], v[98:113]
	v_mfma_f32_32x32x16_f16 v[82:97], v[194:197], v[236:239], v[82:97]
	v_cmp_lt_f32_e32 vcc, v244, v12
	s_cbranch_vccz .LBB1_56

.LBB1_56:
	v_cmp_lt_f32_e32 vcc, v244, v11
	s_cbranch_vccz .LBB1_89
	ds_read_b128 v[12:15], v206 offset:63488
	v_sub_f32_e32 v1, v18, v10
	v_sub_f32_e32 v3, v20, v10
	v_sub_f32_e32 v5, v22, v10
	v_sub_f32_e32 v7, v24, v10
	v_exp_f32_e32 v11, v1
	v_sub_f32_e32 v1, v19, v10
	v_exp_f32_e32 v4, v3
	v_sub_f32_e32 v3, v21, v10
	v_exp_f32_e32 v6, v5
	v_sub_f32_e32 v5, v23, v10
	v_exp_f32_e32 v8, v7
	v_sub_f32_e32 v7, v25, v10
	v_exp_f32_e32 v7, v7
	v_exp_f32_e32 v5, v5
	v_exp_f32_e32 v3, v3
	v_exp_f32_e32 v1, v1
	v_cvt_pk_f16_f32 v239, v8, v7
	v_cvt_pk_f16_f32 v238, v6, v5
	v_cvt_pk_f16_f32 v237, v4, v3
	v_cvt_pk_f16_f32 v236, v11, v1
	s_waitcnt lgkmcnt(0)
	s_nop 0
	v_mfma_f32_32x32x16_f16 v[98:113], v[12:15], v[236:239], v[98:113]
	v_mfma_f32_32x32x16_f16 v[82:97], v[194:197], v[236:239], v[82:97]
	v_cmp_lt_f32_e32 vcc, v244, v9
	s_cbranch_vccz .LBB1_59

.LBB1_82:
	v_mov_b64_e32 v[82:83], 0
	v_mov_b64_e32 v[84:85], 0
	v_mov_b64_e32 v[86:87], 0
	v_mov_b64_e32 v[88:89], 0
	v_mov_b64_e32 v[90:91], 0
	v_mov_b64_e32 v[92:93], 0
	v_mov_b64_e32 v[94:95], 0
	v_mov_b64_e32 v[96:97], 0
	v_mov_b64_e32 v[98:99], 0
	v_mov_b64_e32 v[100:101], 0
	v_mov_b64_e32 v[102:103], 0
	v_mov_b64_e32 v[104:105], 0
	v_mov_b64_e32 v[106:107], 0
	v_mov_b64_e32 v[108:109], 0
	v_mov_b64_e32 v[110:111], 0
	v_mov_b64_e32 v[112:113], 0
	v_cmp_lt_f32_e32 vcc, v244, v243
	s_cbranch_vccnz .LBB1_22
	s_branch .LBB1_23
.LBB1_83:
	v_cmp_lt_f32_e32 vcc, v244, v241
	s_cbranch_vccnz .LBB1_25
	s_branch .LBB1_26
.LBB1_84:
	v_cmp_lt_f32_e32 vcc, v244, v239
	s_cbranch_vccnz .LBB1_28
	s_branch .LBB1_29
.LBB1_85:
	v_cmp_lt_f32_e32 vcc, v244, v237
	s_cbranch_vccnz .LBB1_31
	s_branch .LBB1_32
.LBB1_86:
	v_cmp_lt_f32_e32 vcc, v244, v16
	s_cbranch_vccnz .LBB1_49
	s_branch .LBB1_50
.LBB1_87:
	v_cmp_lt_f32_e32 vcc, v244, v14
	s_cbranch_vccnz .LBB1_52
	s_branch .LBB1_53
.LBB1_88:
	v_cmp_lt_f32_e32 vcc, v244, v12
	s_cbranch_vccnz .LBB1_55
	s_branch .LBB1_56
.LBB1_89:
	v_cmp_lt_f32_e32 vcc, v244, v9
	s_cbranch_vccnz .LBB1_58
	s_branch .LBB1_59
